# GEMM2 LayerNorm-1 statistics exchange: L1 invalidate issued before the counter poll instead of after it
# speedup vs baseline: 1.0048x; 1.0048x over previous
;     __device__ __forceinline__ bool run(const f32x4 (&v)[2][2][4][2], const Unit& u, int wr, int wc, int fr, int fq, PG8_LAS unsigned char* lds, int wid, int lane) const {
;     ...
;         if (wid == 0) {
;             bool dead = false; const unsigned long long t0 = __builtin_amdgcn_s_memrealtime(); const unsigned want = 8u * (unsigned)ntn;
;             for (;;) {
;     ...
;                 break;
;     ...
;                 if ((unsigned)__builtin_amdgcn_readfirstlane(__hip_atomic_load(cnt + 64 * u.pm, __ATOMIC_RELAXED, __HIP_MEMORY_SCOPE_AGENT)) >= want) break;
;                 if (__builtin_amdgcn_s_memrealtime() - t0 > 2000000ull) {
.LBB0_473:
	s_or_b64 exec, exec, s[20:21]
	s_cmp_gt_u32 s49, 63
	s_cbranch_scc1 .LBB0_490
	s_memrealtime s[20:21]
	buffer_inv sc1
	s_lshl_b32 s22, s16, 6
	s_ashr_i32 s23, s22, 31
	s_lshl_b64 s[22:23], s[22:23], 2
	s_add_u32 s22, s17, s22
	s_addc_u32 s23, s24, s23
	v_mov_b32_e32 v135, 0
	v_mov_b64_e32 v[132:133], 0x1e8481
	s_branch .LBB0_477

;     __device__ __forceinline__ bool run(const f32x4 (&v)[2][2][4][2], const Unit& u, int wr, int wc, int fr, int fq, PG8_LAS unsigned char* lds, int wid, int lane) const {
;     ...
;                 if (__builtin_amdgcn_s_memrealtime() - t0 > 2000000ull) {
;                     if (lane == 0) { unsigned expect = 0u; __hip_atomic_compare_exchange_strong(tmo + 1, &expect, code | (unsigned)(u.pm & 0xff), __ATOMIC_RELAXED, __ATOMIC_RELAXED, __HIP_MEMORY_SCOPE_AGENT);
;                                      __hip_atomic_store(tmo, 1u, __ATOMIC_RELAXED, __HIP_MEMORY_SCOPE_AGENT); }
;                     dead = true; break; }
.LBB0_480:
	s_andn2_b64 vcc, exec, s[24:25]
	s_cbranch_vccz .LBB0_486
	s_waitcnt lgkmcnt(0)
	s_and_saveexec_b64 s[20:21], s[8:9]
	s_xor_b64 s[8:9], exec, s[20:21]
	s_cbranch_execz .LBB0_483
.LBB0_483:
	s_or_saveexec_b64 s[20:21], s[8:9]
	s_mov_b64 s[8:9], 0
	s_xor_b64 exec, exec, s[20:21]
	s_cbranch_execz .LBB0_485
	s_and_b32 s16, s16, 0xff
	s_or_b32 s16, s16, 0x700
	v_mov_b32_e32 v133, 0
	v_mov_b32_e32 v132, s16
	global_atomic_cmpswap v133, v[132:133], s[30:31] offset:4
	s_mov_b64 s[8:9], exec
	v_mov_b32_e32 v132, 1
	global_store_dword v133, v132, s[30:31] sc1

;     __device__ __forceinline__ bool run(const f32x4 (&v)[2][2][4][2], const Unit& u, int wr, int wc, int fr, int fq, PG8_LAS unsigned char* lds, int wid, int lane) const {
;     ...
;             __builtin_amdgcn_fence(__ATOMIC_ACQUIRE, "agent");
;             if (lane == 0) flag[0] = dead ? 1u : 0u;
.LBB0_487:
	s_waitcnt vmcnt(0)
	s_and_b64 exec, exec, s[6:7]
	v_cndmask_b32_e64 v132, 0, 1, s[16:17]
	v_mov_b32_e32 v133, 0
	ds_write_b32 v133, v132 offset:10240

;     __device__ __forceinline__ bool run(const f32x4 (&v)[2][2][4][2], const Unit& u, int wr, int wc, int fr, int fq, PG8_LAS unsigned char* lds, int wid, int lane) const {
;     ...
;                 if (__builtin_amdgcn_s_memrealtime() - t0 > 2000000ull) {
;                     if (lane == 0) { unsigned expect = 0u; __hip_atomic_compare_exchange_strong(tmo + 1, &expect, code | (unsigned)(u.pm & 0xff), __ATOMIC_RELAXED, __ATOMIC_RELAXED, __HIP_MEMORY_SCOPE_AGENT);
;                                      __hip_atomic_store(tmo, 1u, __ATOMIC_RELAXED, __HIP_MEMORY_SCOPE_AGENT); }
;                     dead = true; break; }
.LBB0_1476:
	s_andn2_b64 vcc, exec, s[24:25]
	s_cbranch_vccz .LBB0_1482
	s_waitcnt lgkmcnt(0)
	s_and_saveexec_b64 s[20:21], s[8:9]
	s_xor_b64 s[8:9], exec, s[20:21]
	s_cbranch_execz .LBB0_1479
.LBB0_1479:
	s_or_saveexec_b64 s[20:21], s[8:9]
	s_mov_b64 s[8:9], 0
	s_xor_b64 exec, exec, s[20:21]
	s_cbranch_execz .LBB0_1481
	s_and_b32 s16, s16, 0xbf
	s_or_b32 s16, s16, 0x740
	v_mov_b32_e32 v133, 0
	v_mov_b32_e32 v132, s16
	global_atomic_cmpswap v133, v[132:133], s[30:31] offset:4
	s_mov_b64 s[8:9], exec
	v_mov_b32_e32 v132, 1
	global_store_dword v133, v132, s[30:31] sc1
